# k_iter first: mid-kernel kernarg loads moved to the entry
# baseline (speedup 1.0000x reference)
_Z6k_iterILb1ELb0EEvPKfS1_PKiPK15HIP_vector_typeIfLj4EES7_S1_S1_S3_S1_PfS8_S1_S3_PDF16_PS5_SA_PiSA_SB_:
	s_load_dwordx2 s[4:5], s[0:1], 0x78
	s_load_dwordx8 s[20:27], s[0:1], 0x20
	s_load_dwordx2 s[92:93], s[0:1], 0x18
	s_load_dwordx2 s[48:49], s[0:1], 0x90
	s_load_dwordx2 s[50:51], s[0:1], 0x80
	s_load_dwordx4 s[28:31], s[0:1], 0x60
	v_readfirstlane_b32 s54, v0
	v_cmp_gt_u32_e64 s[8:9], 64, v0
	v_lshlrev_b32_e32 v46, 2, v0
	s_and_saveexec_b64 s[6:7], s[8:9]
	v_mov_b32_e32 v1, 0
	ds_write_b32 v46, v1 offset:29728
	s_or_b64 exec, exec, s[6:7]
	s_lshl_b32 s3, s2, 5
	s_and_b32 s3, s3, 0xe0
	s_lshr_b32 s2, s2, 3
	s_add_i32 s46, s3, s2
	s_lshr_b32 s12, s46, 6
	s_lshl_b32 s13, s46, 6
	s_mov_b32 s47, 0
	s_and_b32 s33, s13, 0xfc0
	s_lshl_b32 s58, s12, 12
	s_lshl_b64 s[2:3], s[46:47], 4
	s_waitcnt lgkmcnt(0)
	s_add_u32 s6, s20, s2
	v_and_b32_e32 v25, 31, v0
	s_addc_u32 s7, s21, s3
	s_or_b32 s59, s58, s33
	v_or_b32_e32 v6, s59, v25
	v_mov_b32_e32 v7, 0
	v_lshlrev_b64 v[2:3], 2, v[6:7]
	v_lshl_add_u64 v[4:5], s[22:23], 0, v[2:3]
	v_lshl_add_u64 v[8:9], s[24:25], 0, v[2:3]
	v_lshl_add_u64 v[2:3], s[26:27], 0, v[2:3]
	global_load_dword v196, v[4:5], off offset:128
	global_load_dword v197, v[8:9], off offset:128
	global_load_dword v198, v[2:3], off offset:128
	global_load_dword v4, v[4:5], off
	global_load_dword v5, v[8:9], off
	global_load_dword v6, v[2:3], off
	s_lshl_b32 s94, s12, 13
	s_add_u32 s94, s92, s94
	s_addc_u32 s95, s93, 0
	v_lshlrev_b32_e32 v199, 4, v0
	global_load_dwordx4 v[192:195], v199, s[94:95]
	s_load_dwordx4 s[36:39], s[6:7], 0x0
	s_load_dwordx2 s[34:35], s[0:1], 0x48
	s_load_dwordx4 s[40:43], s[0:1], 0x0
	s_load_dwordx2 s[52:53], s[0:1], 0x10
	s_load_dwordx2 s[98:99], s[0:1], 0x88
	s_load_dwordx2 s[100:101], s[0:1], 0x58
	s_bfe_u32 s14, s54, 0x10006
	s_cmpk_lt_u32 s54, 0x80
	s_cselect_b64 s[6:7], -1, 0
	s_waitcnt lgkmcnt(0)
	v_mov_b64_e32 v[2:3], s[38:39]
	v_pk_add_f32 v[2:3], s[36:37], v[2:3]
	s_cmp_eq_u32 s14, 0
	v_pk_mul_f32 v[22:23], v[2:3], 0.5 op_sel_hi:[1,0]
	v_and_b32_e32 v44, 63, v0
	s_cselect_b64 s[10:11], -1, 0
	v_mov_b32_e32 v1, 0xff800000
	v_cmp_gt_u32_e64 s[18:19], 32, v44
	s_and_b64 s[10:11], s[10:11], s[6:7]
	s_and_b64 s[16:17], s[10:11], s[18:19]
	v_lshlrev_b32_e32 v10, 4, v25
	s_waitcnt vmcnt(2)
	v_pk_fma_f32 v[36:37], v[2:3], 0.5, v[4:5] op_sel_hi:[1,0,1] neg_lo:[1,0,0] neg_hi:[1,0,0]
	s_nop 0
	v_pk_mul_f32 v[2:3], v[36:37], v[36:37]
	s_waitcnt vmcnt(1)
	v_cmp_ne_u32_e32 vcc, 0, v6
	v_add_f32_e32 v2, v2, v3
	v_sub_f32_e32 v2, 0x3d23d70a, v2
	v_mul_f32_e32 v2, 0x431044f5, v2
	v_cndmask_b32_e32 v4, v1, v2, vcc
	s_and_saveexec_b64 s[10:11], s[16:17]
	s_cbranch_execz .LBB2_4
	s_mov_b32 s16, 0x439044f5
	v_or_b32_e32 v6, s13, v25
	v_pk_mul_f32 v[2:3], v[36:37], s[16:17] op_sel_hi:[1,0]
	v_mov_b32_e32 v5, v7
	v_lshl_add_u64 v[8:9], v[6:7], 4, s[4:5]
	ds_write_b128 v10, v[2:5] offset:26656
	global_store_dwordx4 v[8:9], v[2:5], off sc1

.LBB2_10:
	s_or_b64 exec, exec, s[10:11]
	s_waitcnt lgkmcnt(1)
	v_add_u32_e32 v1, v15, v14
	v_add_u32_e32 v1, v1, v16
	v_add_u32_e32 v1, v1, v17
	s_waitcnt lgkmcnt(0)
	v_add_u32_e32 v1, v1, v10
	v_add_u32_e32 v1, v1, v11
	v_add_u32_e32 v1, v1, v12
	v_add_u32_e32 v1, v1, v13
	s_lshr_b32 s27, s54, 6
	v_readfirstlane_b32 s2, v1
	s_lshl_b32 s60, s2, 3
	s_lshl_b64 s[20:21], s[46:47], 16
	s_add_u32 s44, s6, s20
	s_addc_u32 s45, s7, s21
	s_cmp_lt_i32 s2, 1
	s_waitcnt lgkmcnt(0)
	s_barrier
	s_cbranch_scc1 .LBB2_20
	s_lshl_b32 s47, s27, 2
	s_addk_i32 s47, 0x6000
	s_cmpk_gt_u32 s54, 0x1ff
	s_cselect_b64 s[2:3], -1, 0
	s_cmpk_gt_u32 s54, 0x1bf
	s_cselect_b64 s[4:5], -1, 0
	s_cmpk_gt_u32 s54, 0x17f
	s_cselect_b64 s[6:7], -1, 0
	s_cmpk_gt_u32 s54, 0x13f
	s_cselect_b64 s[10:11], -1, 0
	s_cmpk_gt_u32 s54, 0xff
	s_cselect_b64 s[12:13], -1, 0
	s_cmpk_gt_u32 s54, 0xbf
	s_cselect_b64 s[14:15], -1, 0
	s_cmpk_gt_u32 s54, 0x7f
	s_cselect_b64 s[16:17], -1, 0
	s_cmp_lt_u32 s54, 64
	s_cselect_b64 s[54:55], -1, 0
	s_waitcnt lgkmcnt(0)
	s_add_u32 s20, s98, s20
	v_mov_b32_e32 v7, 0
	s_addc_u32 s21, s99, s21
	v_lshl_add_u64 v[10:11], s[20:21], 0, v[6:7]
	v_and_b32_e32 v5, 7, v0
	v_not_b32_e32 v1, v19
	v_not_b32_e32 v24, v18
	v_lshl_add_u64 v[26:27], v[10:11], 0, 8
	v_lshrrev_b32_e32 v9, 3, v0
	s_mov_b32 s61, 0
	s_mov_b32 s62, 0x3d23dc48
	s_movk_i32 s63, 0x600
	s_mov_b64 s[56:57], 0x2000
	v_mov_b32_e32 v30, 0xff800000
	v_mov_b32_e32 v6, 0
	s_mov_b32 s91, 0

.LBB2_21:
	s_mov_b64 s[20:21], s[100:101]
	s_lshl_b32 s66, s27, 3
	s_add_i32 s66, s59, s66
	s_mov_b32 s67, 0
	s_lshl_b64 s[66:67], s[66:67], 2
	s_add_u32 s66, s28, s66
	s_addc_u32 s67, s29, s67
	s_load_dwordx8 s[68:75], s[66:67], 0x0
	v_readfirstlane_b32 s38, v6
	v_cmp_eq_u32_e64 s[14:15], 0, v0
	s_and_saveexec_b64 s[0:1], s[14:15]
	s_cbranch_execz .LBB2_23
	s_lshl_b32 s2, s46, 2
	v_mov_b32_e32 v1, s2
	v_mov_b32_e32 v5, s38
	global_store_dword v1, v5, s[50:51]
	v_mov_b32_e32 v5, s60
	global_store_dword v1, v5, s[48:49]

	.amdhsa_kernel _Z6k_iterILb1ELb0EEvPKfS1_PKiPK15HIP_vector_typeIfLj4EES7_S1_S1_S3_S1_PfS8_S1_S3_PDF16_PS5_SA_PiSA_SB_
		.amdhsa_group_segment_fixed_size 30384
		.amdhsa_private_segment_fixed_size 0
		.amdhsa_kernarg_size 152
		.amdhsa_user_sgpr_count 2
		.amdhsa_user_sgpr_dispatch_ptr 0
		.amdhsa_user_sgpr_queue_ptr 0
		.amdhsa_user_sgpr_kernarg_segment_ptr 1
		.amdhsa_user_sgpr_dispatch_id 0
		.amdhsa_user_sgpr_kernarg_preload_length 0
		.amdhsa_user_sgpr_kernarg_preload_offset 0
		.amdhsa_user_sgpr_private_segment_size 0
		.amdhsa_uses_dynamic_stack 0
		.amdhsa_enable_private_segment 0
		.amdhsa_system_sgpr_workgroup_id_x 1
		.amdhsa_system_sgpr_workgroup_id_y 0
		.amdhsa_system_sgpr_workgroup_id_z 0
		.amdhsa_system_sgpr_workgroup_info 0
		.amdhsa_system_vgpr_workitem_id 0
		.amdhsa_next_free_vgpr 256
		.amdhsa_next_free_sgpr 102
		.amdhsa_accum_offset 256
		.amdhsa_reserve_vcc 1
		.amdhsa_float_round_mode_32 0
		.amdhsa_float_round_mode_16_64 0
		.amdhsa_float_denorm_mode_32 3
		.amdhsa_float_denorm_mode_16_64 3
		.amdhsa_dx10_clamp 1
		.amdhsa_ieee_mode 1
		.amdhsa_fp16_overflow 0
		.amdhsa_tg_split 0
		.amdhsa_exception_fp_ieee_invalid_op 0
		.amdhsa_exception_fp_denorm_src 0
		.amdhsa_exception_fp_ieee_div_zero 0
		.amdhsa_exception_fp_ieee_overflow 0
		.amdhsa_exception_fp_ieee_underflow 0
		.amdhsa_exception_fp_ieee_inexact 0
		.amdhsa_exception_int_div_zero 0
	.end_amdhsa_kernel

amdhsa.kernels:
  - .agpr_count:     0
    .args:
      - .actual_access:  read_only
        .address_space:  global
        .offset:         0
        .size:           8
        .value_kind:     global_buffer
      - .actual_access:  read_only
        .address_space:  global
        .offset:         8
        .size:           8
        .value_kind:     global_buffer
      - .actual_access:  read_only
        .address_space:  global
        .offset:         16
        .size:           8
        .value_kind:     global_buffer
      - .actual_access:  read_only
        .address_space:  global
        .offset:         24
        .size:           8
        .value_kind:     global_buffer
      - .actual_access:  write_only
        .address_space:  global
        .offset:         32
        .size:           8
        .value_kind:     global_buffer
      - .actual_access:  write_only
        .address_space:  global
        .offset:         40
        .size:           8
        .value_kind:     global_buffer
      - .actual_access:  write_only
        .address_space:  global
        .offset:         48
        .size:           8
        .value_kind:     global_buffer
      - .actual_access:  write_only
        .address_space:  global
        .offset:         56
        .size:           8
        .value_kind:     global_buffer
      - .actual_access:  write_only
        .address_space:  global
        .offset:         64
        .size:           8
        .value_kind:     global_buffer
      - .actual_access:  write_only
        .address_space:  global
        .offset:         72
        .size:           8
        .value_kind:     global_buffer
      - .actual_access:  write_only
        .address_space:  global
        .offset:         80
        .size:           8
        .value_kind:     global_buffer
      - .actual_access:  write_only
        .address_space:  global
        .offset:         88
        .size:           8
        .value_kind:     global_buffer
      - .actual_access:  write_only
        .address_space:  global
        .offset:         96
        .size:           8
        .value_kind:     global_buffer
      - .actual_access:  write_only
        .address_space:  global
        .offset:         104
        .size:           8
        .value_kind:     global_buffer
      - .actual_access:  write_only
        .address_space:  global
        .offset:         112
        .size:           8
        .value_kind:     global_buffer
    .group_segment_fixed_size: 67584
    .kernarg_segment_align: 8
    .kernarg_segment_size: 120
    .language:       OpenCL C
    .language_version:
      - 2
      - 0
    .max_flat_workgroup_size: 1024
    .name:           _Z6k_sortPKfS0_PKiS2_PiP15HIP_vector_typeIfLj4EEPfS7_S3_S7_S7_S3_S3_S6_S6_
    .private_segment_fixed_size: 0
    .sgpr_count:     58
    .sgpr_spill_count: 0
    .symbol:         _Z6k_sortPKfS0_PKiS2_PiP15HIP_vector_typeIfLj4EEPfS7_S3_S7_S7_S3_S3_S6_S6_.kd
    .uniform_work_group_size: 1
    .uses_dynamic_stack: false
    .vgpr_count:     48
    .vgpr_spill_count: 0
    .wavefront_size: 64
  - .agpr_count:     0
    .args:
      - .actual_access:  read_only
        .address_space:  global
        .offset:         0
        .size:           8
        .value_kind:     global_buffer
      - .actual_access:  read_only
        .address_space:  global
        .offset:         8
        .size:           8
        .value_kind:     global_buffer
      - .actual_access:  read_only
        .address_space:  global
        .offset:         16
        .size:           8
        .value_kind:     global_buffer
      - .actual_access:  read_only
        .address_space:  global
        .offset:         24
        .size:           8
        .value_kind:     global_buffer
      - .actual_access:  read_only
        .address_space:  global
        .offset:         32
        .size:           8
        .value_kind:     global_buffer
      - .actual_access:  read_only
        .address_space:  global
        .offset:         40
        .size:           8
        .value_kind:     global_buffer
      - .actual_access:  read_only
        .address_space:  global
        .offset:         48
        .size:           8
        .value_kind:     global_buffer
      - .actual_access:  write_only
        .address_space:  global
        .offset:         56
        .size:           8
        .value_kind:     global_buffer
    .group_segment_fixed_size: 145952
    .kernarg_segment_align: 8
    .kernarg_segment_size: 64
    .language:       OpenCL C
    .language_version:
      - 2
      - 0
    .max_flat_workgroup_size: 512
    .name:           _Z7k_finalPK15HIP_vector_typeIfLj4EES2_PKiS4_PKfS6_PKDF16_Pf
    .private_segment_fixed_size: 0
    .sgpr_count:     34
    .sgpr_spill_count: 0
    .symbol:         _Z7k_finalPK15HIP_vector_typeIfLj4EES2_PKiS4_PKfS6_PKDF16_Pf.kd
    .uniform_work_group_size: 1
    .uses_dynamic_stack: false
    .vgpr_count:     177
    .vgpr_spill_count: 0
    .wavefront_size: 64
  - .agpr_count:     0
    .args:
      - .actual_access:  read_only
        .address_space:  global
        .offset:         0
        .size:           8
        .value_kind:     global_buffer
      - .actual_access:  read_only
        .address_space:  global
        .offset:         8
        .size:           8
        .value_kind:     global_buffer
      - .actual_access:  read_only
        .address_space:  global
        .offset:         16
        .size:           8
        .value_kind:     global_buffer
      - .actual_access:  read_only
        .address_space:  global
        .offset:         24
        .size:           8
        .value_kind:     global_buffer
      - .actual_access:  read_only
        .address_space:  global
        .offset:         32
        .size:           8
        .value_kind:     global_buffer
      - .actual_access:  read_only
        .address_space:  global
        .offset:         40
        .size:           8
        .value_kind:     global_buffer
      - .actual_access:  read_only
        .address_space:  global
        .offset:         48
        .size:           8
        .value_kind:     global_buffer
      - .actual_access:  read_only
        .address_space:  global
        .offset:         56
        .size:           8
        .value_kind:     global_buffer
      - .actual_access:  read_only
        .address_space:  global
        .offset:         64
        .size:           8
        .value_kind:     global_buffer
      - .address_space:  global
        .offset:         72
        .size:           8
        .value_kind:     global_buffer
      - .actual_access:  read_only
        .address_space:  global
        .offset:         80
        .size:           8
        .value_kind:     global_buffer
      - .actual_access:  read_only
        .address_space:  global
        .offset:         88
        .size:           8
        .value_kind:     global_buffer
      - .actual_access:  read_only
        .address_space:  global
        .offset:         96
        .size:           8
        .value_kind:     global_buffer
      - .actual_access:  write_only
        .address_space:  global
        .offset:         104
        .size:           8
        .value_kind:     global_buffer
      - .address_space:  global
        .offset:         112
        .size:           8
        .value_kind:     global_buffer
      - .actual_access:  write_only
        .address_space:  global
        .offset:         120
        .size:           8
        .value_kind:     global_buffer
      - .actual_access:  write_only
        .address_space:  global
        .offset:         128
        .size:           8
        .value_kind:     global_buffer
      - .actual_access:  write_only
        .address_space:  global
        .offset:         136
        .size:           8
        .value_kind:     global_buffer
      - .actual_access:  write_only
        .address_space:  global
        .offset:         144
        .size:           8
        .value_kind:     global_buffer
    .group_segment_fixed_size: 30384
    .kernarg_segment_align: 8
    .kernarg_segment_size: 152
    .language:       OpenCL C
    .language_version:
      - 2
      - 0
    .max_flat_workgroup_size: 512
    .name:           _Z6k_iterILb1ELb0EEvPKfS1_PKiPK15HIP_vector_typeIfLj4EES7_S1_S1_S3_S1_PfS8_S1_S3_PDF16_PS5_SA_PiSA_SB_
    .private_segment_fixed_size: 0
    .sgpr_count:     108
    .sgpr_spill_count: 0
    .symbol:         _Z6k_iterILb1ELb0EEvPKfS1_PKiPK15HIP_vector_typeIfLj4EES7_S1_S1_S3_S1_PfS8_S1_S3_PDF16_PS5_SA_PiSA_SB_.kd
    .uniform_work_group_size: 1
    .uses_dynamic_stack: false
    .vgpr_count:     256
    .vgpr_spill_count: 0
    .wavefront_size: 64
  - .agpr_count:     0
    .args:
      - .actual_access:  read_only
        .address_space:  global
        .offset:         0
        .size:           8
        .value_kind:     global_buffer
      - .actual_access:  read_only
        .address_space:  global
        .offset:         8
        .size:           8
        .value_kind:     global_buffer
      - .actual_access:  read_only
        .address_space:  global
        .offset:         16
        .size:           8
        .value_kind:     global_buffer
      - .actual_access:  read_only
        .address_space:  global
        .offset:         24
        .size:           8
        .value_kind:     global_buffer
      - .actual_access:  read_only
        .address_space:  global
        .offset:         32
        .size:           8
        .value_kind:     global_buffer
      - .actual_access:  read_only
        .address_space:  global
        .offset:         40
        .size:           8
        .value_kind:     global_buffer
      - .actual_access:  read_only
        .address_space:  global
        .offset:         48
        .size:           8
        .value_kind:     global_buffer
      - .actual_access:  read_only
        .address_space:  global
        .offset:         56
        .size:           8
        .value_kind:     global_buffer
      - .actual_access:  read_only
        .address_space:  global
        .offset:         64
        .size:           8
        .value_kind:     global_buffer
      - .address_space:  global
        .offset:         72
        .size:           8
        .value_kind:     global_buffer
      - .actual_access:  read_only
        .address_space:  global
        .offset:         80
        .size:           8
        .value_kind:     global_buffer
      - .actual_access:  read_only
        .address_space:  global
        .offset:         88
        .size:           8
        .value_kind:     global_buffer
      - .actual_access:  read_only
        .address_space:  global
        .offset:         96
        .size:           8
        .value_kind:     global_buffer
      - .actual_access:  read_only
        .address_space:  global
        .offset:         104
        .size:           8
        .value_kind:     global_buffer
      - .actual_access:  read_only
        .address_space:  global
        .offset:         112
        .size:           8
        .value_kind:     global_buffer
      - .actual_access:  read_only
        .address_space:  global
        .offset:         120
        .size:           8
        .value_kind:     global_buffer
      - .actual_access:  read_only
        .address_space:  global
        .offset:         128
        .size:           8
        .value_kind:     global_buffer
      - .actual_access:  read_only
        .address_space:  global
        .offset:         136
        .size:           8
        .value_kind:     global_buffer
      - .actual_access:  read_only
        .address_space:  global
        .offset:         144
        .size:           8
        .value_kind:     global_buffer
    .group_segment_fixed_size: 5808
    .kernarg_segment_align: 8
    .kernarg_segment_size: 152
    .language:       OpenCL C
    .language_version:
      - 2
      - 0
    .max_flat_workgroup_size: 512
    .name:           _Z6k_iterILb0ELb0EEvPKfS1_PKiPK15HIP_vector_typeIfLj4EES7_S1_S1_S3_S1_PfS8_S1_S3_PDF16_PS5_SA_PiSA_SB_
    .private_segment_fixed_size: 0
    .sgpr_count:     46
    .sgpr_spill_count: 0
    .symbol:         _Z6k_iterILb0ELb0EEvPKfS1_PKiPK15HIP_vector_typeIfLj4EES7_S1_S1_S3_S1_PfS8_S1_S3_PDF16_PS5_SA_PiSA_SB_.kd
    .uniform_work_group_size: 1
    .uses_dynamic_stack: false
    .vgpr_count:     184
    .vgpr_spill_count: 0
    .wavefront_size: 64
  - .agpr_count:     0
    .args:
      - .actual_access:  read_only
        .address_space:  global
        .offset:         0
        .size:           8
        .value_kind:     global_buffer
      - .actual_access:  read_only
        .address_space:  global
        .offset:         8
        .size:           8
        .value_kind:     global_buffer
      - .actual_access:  read_only
        .address_space:  global
        .offset:         16
        .size:           8
        .value_kind:     global_buffer
      - .actual_access:  read_only
        .address_space:  global
        .offset:         24
        .size:           8
        .value_kind:     global_buffer
      - .actual_access:  read_only
        .address_space:  global
        .offset:         32
        .size:           8
        .value_kind:     global_buffer
      - .actual_access:  read_only
        .address_space:  global
        .offset:         40
        .size:           8
        .value_kind:     global_buffer
      - .actual_access:  read_only
        .address_space:  global
        .offset:         48
        .size:           8
        .value_kind:     global_buffer
      - .actual_access:  read_only
        .address_space:  global
        .offset:         56
        .size:           8
        .value_kind:     global_buffer
      - .actual_access:  read_only
        .address_space:  global
        .offset:         64
        .size:           8
        .value_kind:     global_buffer
      - .address_space:  global
        .offset:         72
        .size:           8
        .value_kind:     global_buffer
      - .actual_access:  write_only
        .address_space:  global
        .offset:         80
        .size:           8
        .value_kind:     global_buffer
      - .actual_access:  read_only
        .address_space:  global
        .offset:         88
        .size:           8
        .value_kind:     global_buffer
      - .actual_access:  read_only
        .address_space:  global
        .offset:         96
        .size:           8
        .value_kind:     global_buffer
      - .actual_access:  read_only
        .address_space:  global
        .offset:         104
        .size:           8
        .value_kind:     global_buffer
      - .actual_access:  read_only
        .address_space:  global
        .offset:         112
        .size:           8
        .value_kind:     global_buffer
      - .actual_access:  read_only
        .address_space:  global
        .offset:         120
        .size:           8
        .value_kind:     global_buffer
      - .actual_access:  read_only
        .address_space:  global
        .offset:         128
        .size:           8
        .value_kind:     global_buffer
      - .actual_access:  read_only
        .address_space:  global
        .offset:         136
        .size:           8
        .value_kind:     global_buffer
      - .actual_access:  read_only
        .address_space:  global
        .offset:         144
        .size:           8
        .value_kind:     global_buffer
    .group_segment_fixed_size: 5808
    .kernarg_segment_align: 8
    .kernarg_segment_size: 152
    .language:       OpenCL C
    .language_version:
      - 2
      - 0
    .max_flat_workgroup_size: 512
    .name:           _Z6k_iterILb0ELb1EEvPKfS1_PKiPK15HIP_vector_typeIfLj4EES7_S1_S1_S3_S1_PfS8_S1_S3_PDF16_PS5_SA_PiSA_SB_
    .private_segment_fixed_size: 0
    .sgpr_count:     46
    .sgpr_spill_count: 0
    .symbol:         _Z6k_iterILb0ELb1EEvPKfS1_PKiPK15HIP_vector_typeIfLj4EES7_S1_S1_S3_S1_PfS8_S1_S3_PDF16_PS5_SA_PiSA_SB_.kd
    .uniform_work_group_size: 1
    .uses_dynamic_stack: false
    .vgpr_count:     184
    .vgpr_spill_count: 0
    .wavefront_size: 64
